# grid barrier (31 inline copies): single-hop release - every XCD leader adds to all 8 per-XCD completion counters, all WGs poll their XCD's counter >= (r+1)*nx; returning TOP atomic/TOPGEN/relay bypass
# baseline (speedup 1.0000x reference)
; __device__ __forceinline__ unsigned xb_ld(unsigned* p)              { return __hip_atomic_load(p, __ATOMIC_RELAXED, __HIP_MEMORY_SCOPE_AGENT); }
; __device__ __forceinline__ unsigned xb_add(unsigned* p, unsigned v) { return __hip_atomic_fetch_add(p, v, __ATOMIC_RELAXED, __HIP_MEMORY_SCOPE_AGENT); }
; #define XB_SPIN(cond, bar) do { unsigned _sp = 0; while (cond) { __builtin_amdgcn_s_sleep(1); \
;     if ((++_sp & 255u) == 0u) { if (xb_ld(&(bar)[XB_TMO])) break; if (_sp > XB_SPIN_CAP) { atomicAdd(&(bar)[XB_TMO], 1u); break; } } } } while (0)
; __device__ __forceinline__ void xcd_barrier(const XcdBarrier& b) {
;     ...
;         unsigned nloc = b.st[0], nx = b.st[1];
;         if (nloc == 0u) { xcd_barrier_complete(bar, b.x, nloc, nx); b.st[0] = nloc; b.st[1] = nx; }
;         const unsigned old = xb_add(&bar[XB_XSUB(b.x)], 1u);
;         const unsigned gen = old / nloc;
;         if (old + 1u == (gen + 1u) * nloc) {
;             __builtin_amdgcn_fence(__ATOMIC_RELEASE, "agent");
;             asm volatile("s_waitcnt vmcnt(0)" ::: "memory");
;             const unsigned og = xb_add(&bar[XB_TOP], 1u);
;             const unsigned tg = og / nx;
;             if (og + 1u == (tg + 1u) * nx) xb_add(&bar[XB_TOPGEN], 1u);
;             else XB_SPIN(xb_ld(&bar[XB_TOPGEN]) == tg, bar);
;             __builtin_amdgcn_fence(__ATOMIC_ACQUIRE, "agent");
;             xb_add(&bar[XB_XGEN(b.x)], 1u);
;             asm volatile("s_waitcnt vmcnt(0)" ::: "memory");
;         } else {
;             XB_SPIN(xb_ld(&bar[XB_XGEN(b.x)]) == gen, bar);
;             __builtin_amdgcn_fence(__ATOMIC_ACQUIRE, "agent");
;             asm volatile("s_waitcnt vmcnt(0)" ::: "memory");
.LBB0_65:
	v_readlane_b32 s2, v253, 6
	s_lshl_b32 s2, s2, 8
	v_readlane_b32 s4, v253, 4
	v_readlane_b32 s5, v253, 5
	s_add_u32 s2, s4, s2
	s_addc_u32 s3, s5, 0
	v_mov_b32_e32 v2, 0x1000
	v_mov_b32_e32 v4, 1
	global_atomic_add v4, v2, v4, s[2:3] offset:1024 sc0
	v_cvt_f32_u32_e32 v2, v3
	v_sub_u32_e32 v5, 0, v3
	v_rcp_iflag_f32_e32 v2, v2
	s_nop 0
	v_mul_f32_e32 v2, 0x4f7ffffe, v2
	v_cvt_u32_f32_e32 v2, v2
	v_mul_lo_u32 v5, v5, v2
	v_mul_hi_u32 v5, v2, v5
	v_add_u32_e32 v2, v2, v5
	s_waitcnt vmcnt(0)
	v_mul_hi_u32 v2, v4, v2
	v_mul_lo_u32 v5, v2, v3
	v_sub_u32_e32 v5, v4, v5
	v_add_u32_e32 v6, 1, v2
	v_cmp_ge_u32_e32 vcc, v5, v3
	v_add_u32_e32 v4, 1, v4
	s_nop 0
	v_cndmask_b32_e32 v2, v2, v6, vcc
	v_sub_u32_e32 v6, v5, v3
	v_cndmask_b32_e32 v5, v5, v6, vcc
	v_add_u32_e32 v6, 1, v2
	v_cmp_ge_u32_e32 vcc, v5, v3
	s_nop 1
	v_cndmask_b32_e32 v2, v2, v6, vcc
	v_mul_lo_u32 v5, v3, v2
	v_add_u32_e32 v3, v5, v3
	v_cmp_ne_u32_e32 vcc, v4, v3
	s_and_saveexec_b64 s[4:5], vcc
	s_xor_b64 s[4:5], exec, s[4:5]
	s_cbranch_execz .LBB0_79
	s_waitcnt lgkmcnt(0)
	v_mov_b32_e32 v2, 0x23fc8
	ds_read_b32 v4, v2
	s_waitcnt lgkmcnt(0)
	v_add_u32_e32 v4, 1, v4
	ds_write_b32 v2, v4
	v_mul_u32_u24_e32 v2, v4, v1
	v_mov_b32_e32 v1, 0x3200
	buffer_inv sc1
	global_load_dword v1, v1, s[2:3] offset:1024 sc1
	s_add_u32 s10, s2, 0x3600
	s_addc_u32 s11, s3, 0
	s_waitcnt vmcnt(0)
	v_cmp_gt_u32_e32 vcc, v2, v1
	s_and_saveexec_b64 s[6:7], vcc
	s_cbranch_execz .LBB0_78
	s_add_u32 s8, s94, 0x4200
	s_addc_u32 s9, s95, 0
	s_mov_b32 s22, 1
	s_mov_b64 s[12:13], 0
	v_mov_b32_e32 v1, 0
	s_branch .LBB0_69

; __device__ __forceinline__ unsigned xb_ld(unsigned* p)              { return __hip_atomic_load(p, __ATOMIC_RELAXED, __HIP_MEMORY_SCOPE_AGENT); }
; #define XB_SPIN(cond, bar) do { unsigned _sp = 0; while (cond) { __builtin_amdgcn_s_sleep(1); \
;     if ((++_sp & 255u) == 0u) { if (xb_ld(&(bar)[XB_TMO])) break; if (_sp > XB_SPIN_CAP) { atomicAdd(&(bar)[XB_TMO], 1u); break; } } } } while (0)
; __device__ __forceinline__ void xcd_barrier(const XcdBarrier& b) {
;     ...
;             XB_SPIN(xb_ld(&bar[XB_XGEN(b.x)]) == gen, bar);
.LBB0_73:
	global_load_dword v3, v1, s[10:11] sc1
	s_add_i32 s22, s22, 1
	s_mov_b64 s[18:19], -1
	s_waitcnt vmcnt(0)
	v_cmp_le_u32_e32 vcc, v2, v3
	s_orn2_b64 s[16:17], vcc, exec
	s_branch .LBB0_68

; __device__ __forceinline__ unsigned xb_ld(unsigned* p)              { return __hip_atomic_load(p, __ATOMIC_RELAXED, __HIP_MEMORY_SCOPE_AGENT); }
; __device__ __forceinline__ unsigned xb_add(unsigned* p, unsigned v) { return __hip_atomic_fetch_add(p, v, __ATOMIC_RELAXED, __HIP_MEMORY_SCOPE_AGENT); }
; #define XB_SPIN(cond, bar) do { unsigned _sp = 0; while (cond) { __builtin_amdgcn_s_sleep(1); \
;     if ((++_sp & 255u) == 0u) { if (xb_ld(&(bar)[XB_TMO])) break; if (_sp > XB_SPIN_CAP) { atomicAdd(&(bar)[XB_TMO], 1u); break; } } } } while (0)
; __device__ __forceinline__ void xcd_barrier(const XcdBarrier& b) {
;     ...
;         const unsigned old = xb_add(&bar[XB_XSUB(b.x)], 1u);
;         const unsigned gen = old / nloc;
;         if (old + 1u == (gen + 1u) * nloc) {
;             __builtin_amdgcn_fence(__ATOMIC_RELEASE, "agent");
;             asm volatile("s_waitcnt vmcnt(0)" ::: "memory");
;             const unsigned og = xb_add(&bar[XB_TOP], 1u);
;             const unsigned tg = og / nx;
;             if (og + 1u == (tg + 1u) * nx) xb_add(&bar[XB_TOPGEN], 1u);
;             else XB_SPIN(xb_ld(&bar[XB_TOPGEN]) == tg, bar);
;             __builtin_amdgcn_fence(__ATOMIC_ACQUIRE, "agent");
;             xb_add(&bar[XB_XGEN(b.x)], 1u);
;             asm volatile("s_waitcnt vmcnt(0)" ::: "memory");
.LBB0_79:
	s_andn2_saveexec_b64 s[4:5], s[4:5]
	s_cbranch_execz .LBB0_97
	s_mov_b64 s[4:5], exec
	buffer_wbl2 sc1
	buffer_inv sc1
	s_waitcnt lgkmcnt(0)
	s_waitcnt vmcnt(0)
	v_mov_b32_e32 v4, 0x23fc8
	ds_read_b32 v3, v4
	s_getreg_b32 s4, hwreg(HW_REG_XCC_ID, 0, 4)
	s_lshl_b32 s4, s4, 8
	s_waitcnt lgkmcnt(0)
	v_add_u32_e32 v3, 1, v3
	ds_write_b32 v4, v3
	v_mul_u32_u24_e32 v3, v3, v1
	v_mov_b32_e32 v4, s4
	v_sub_u32_e32 v4, 0x3600, v4
	v_mov_b32_e32 v5, 1
	global_atomic_add v4, v5, s[2:3]
	global_atomic_add v4, v5, s[2:3] offset:256
	global_atomic_add v4, v5, s[2:3] offset:512
	global_atomic_add v4, v5, s[2:3] offset:768
	global_atomic_add v4, v5, s[2:3] offset:1024
	global_atomic_add v4, v5, s[2:3] offset:1280
	global_atomic_add v4, v5, s[2:3] offset:1536
	global_atomic_add v4, v5, s[2:3] offset:1792
	s_nop 1
	v_add_u32_e32 v5, 1, v2
	v_mov_b32_e32 v4, 0x2000
	global_atomic_umax v4, v5, s[2:3] offset:1024
	s_nop 1
	v_mov_b32_e32 v4, 0x3200
	s_mov_b32 s5, 0
.Lxb_spin_0:
	global_load_dword v5, v4, s[2:3] offset:1024 sc1
	s_add_i32 s5, s5, 1
	s_waitcnt vmcnt(0)
	v_cmp_gt_u32_e32 vcc, v3, v5
	s_cbranch_vccz .Lxb_done_0
	s_cmp_lt_u32 s5, 0x40000
	s_cbranch_scc0 .Lxb_done_0
	s_sleep 1
	s_branch .Lxb_spin_0
.Lxb_done_0:
	s_branch .LBB0_97
	v_mbcnt_lo_u32_b32 v2, s4, 0
	v_mbcnt_hi_u32_b32 v2, s5, v2
	v_cmp_eq_u32_e32 vcc, 0, v2
	s_and_saveexec_b64 s[6:7], vcc
	s_cbranch_execz .LBB0_82
	s_bcnt1_i32_b64 s4, s[4:5]
	v_mov_b32_e32 v3, 0x7000
	v_mov_b32_e32 v4, s4
	global_atomic_add v3, v3, v4, s[94:95] offset:1024 sc0

; __device__ __forceinline__ unsigned xb_ld(unsigned* p)              { return __hip_atomic_load(p, __ATOMIC_RELAXED, __HIP_MEMORY_SCOPE_AGENT); }
; __device__ __forceinline__ unsigned xb_add(unsigned* p, unsigned v) { return __hip_atomic_fetch_add(p, v, __ATOMIC_RELAXED, __HIP_MEMORY_SCOPE_AGENT); }
; #define XB_SPIN(cond, bar) do { unsigned _sp = 0; while (cond) { __builtin_amdgcn_s_sleep(1); \
;     if ((++_sp & 255u) == 0u) { if (xb_ld(&(bar)[XB_TMO])) break; if (_sp > XB_SPIN_CAP) { atomicAdd(&(bar)[XB_TMO], 1u); break; } } } } while (0)
; __device__ __forceinline__ void xcd_barrier(const XcdBarrier& b) {
;     ...
;         unsigned nloc = b.st[0], nx = b.st[1];
;         if (nloc == 0u) { xcd_barrier_complete(bar, b.x, nloc, nx); b.st[0] = nloc; b.st[1] = nx; }
;         const unsigned old = xb_add(&bar[XB_XSUB(b.x)], 1u);
;         const unsigned gen = old / nloc;
;         if (old + 1u == (gen + 1u) * nloc) {
;             __builtin_amdgcn_fence(__ATOMIC_RELEASE, "agent");
;             asm volatile("s_waitcnt vmcnt(0)" ::: "memory");
;             const unsigned og = xb_add(&bar[XB_TOP], 1u);
;             const unsigned tg = og / nx;
;             if (og + 1u == (tg + 1u) * nx) xb_add(&bar[XB_TOPGEN], 1u);
;             else XB_SPIN(xb_ld(&bar[XB_TOPGEN]) == tg, bar);
;             __builtin_amdgcn_fence(__ATOMIC_ACQUIRE, "agent");
;             xb_add(&bar[XB_XGEN(b.x)], 1u);
;             asm volatile("s_waitcnt vmcnt(0)" ::: "memory");
;         } else {
;             XB_SPIN(xb_ld(&bar[XB_XGEN(b.x)]) == gen, bar);
;             __builtin_amdgcn_fence(__ATOMIC_ACQUIRE, "agent");
;             asm volatile("s_waitcnt vmcnt(0)" ::: "memory");
.LBB0_226:
	v_readlane_b32 s2, v253, 6
	s_lshl_b32 s2, s2, 8
	v_readlane_b32 s4, v253, 4
	v_readlane_b32 s5, v253, 5
	s_add_u32 s2, s4, s2
	s_addc_u32 s3, s5, 0
	v_mov_b32_e32 v3, 0x1000
	v_mov_b32_e32 v5, 1
	global_atomic_add v5, v3, v5, s[2:3] offset:1024 sc0
	v_cvt_f32_u32_e32 v3, v4
	v_sub_u32_e32 v6, 0, v4
	v_rcp_iflag_f32_e32 v3, v3
	s_nop 0
	v_mul_f32_e32 v3, 0x4f7ffffe, v3
	v_cvt_u32_f32_e32 v3, v3
	v_mul_lo_u32 v6, v6, v3
	v_mul_hi_u32 v6, v3, v6
	v_add_u32_e32 v3, v3, v6
	s_waitcnt vmcnt(0)
	v_mul_hi_u32 v3, v5, v3
	v_mul_lo_u32 v6, v3, v4
	v_sub_u32_e32 v6, v5, v6
	v_add_u32_e32 v7, 1, v3
	v_cmp_ge_u32_e32 vcc, v6, v4
	v_add_u32_e32 v5, 1, v5
	s_nop 0
	v_cndmask_b32_e32 v3, v3, v7, vcc
	v_sub_u32_e32 v7, v6, v4
	v_cndmask_b32_e32 v6, v6, v7, vcc
	v_add_u32_e32 v7, 1, v3
	v_cmp_ge_u32_e32 vcc, v6, v4
	s_nop 1
	v_cndmask_b32_e32 v3, v3, v7, vcc
	v_mul_lo_u32 v6, v4, v3
	v_add_u32_e32 v4, v6, v4
	v_cmp_ne_u32_e32 vcc, v5, v4
	s_and_saveexec_b64 s[4:5], vcc
	s_xor_b64 s[4:5], exec, s[4:5]
	s_cbranch_execz .LBB0_240
	s_waitcnt lgkmcnt(0)
	v_mov_b32_e32 v3, 0x23fc8
	ds_read_b32 v5, v3
	s_waitcnt lgkmcnt(0)
	v_add_u32_e32 v5, 1, v5
	ds_write_b32 v3, v5
	v_mul_u32_u24_e32 v3, v5, v2
	v_mov_b32_e32 v2, 0x3200
	buffer_inv sc1
	global_load_dword v2, v2, s[2:3] offset:1024 sc1
	s_add_u32 s10, s2, 0x3600
	s_addc_u32 s11, s3, 0
	s_waitcnt vmcnt(0)
	v_cmp_gt_u32_e32 vcc, v3, v2
	s_and_saveexec_b64 s[6:7], vcc
	s_cbranch_execz .LBB0_239
	s_add_u32 s8, s94, 0x4200
	s_addc_u32 s9, s95, 0
	s_mov_b32 s22, 1
	s_mov_b64 s[12:13], 0
	v_mov_b32_e32 v2, 0
	s_branch .LBB0_230

; __device__ __forceinline__ unsigned xb_ld(unsigned* p)              { return __hip_atomic_load(p, __ATOMIC_RELAXED, __HIP_MEMORY_SCOPE_AGENT); }
; #define XB_SPIN(cond, bar) do { unsigned _sp = 0; while (cond) { __builtin_amdgcn_s_sleep(1); \
;     if ((++_sp & 255u) == 0u) { if (xb_ld(&(bar)[XB_TMO])) break; if (_sp > XB_SPIN_CAP) { atomicAdd(&(bar)[XB_TMO], 1u); break; } } } } while (0)
; __device__ __forceinline__ void xcd_barrier(const XcdBarrier& b) {
;     ...
;             XB_SPIN(xb_ld(&bar[XB_XGEN(b.x)]) == gen, bar);
.LBB0_234:
	global_load_dword v4, v2, s[10:11] sc1
	s_add_i32 s22, s22, 1
	s_mov_b64 s[18:19], -1
	s_waitcnt vmcnt(0)
	v_cmp_le_u32_e32 vcc, v3, v4
	s_orn2_b64 s[16:17], vcc, exec
	s_branch .LBB0_229

; __device__ __forceinline__ unsigned xb_ld(unsigned* p)              { return __hip_atomic_load(p, __ATOMIC_RELAXED, __HIP_MEMORY_SCOPE_AGENT); }
; __device__ __forceinline__ unsigned xb_add(unsigned* p, unsigned v) { return __hip_atomic_fetch_add(p, v, __ATOMIC_RELAXED, __HIP_MEMORY_SCOPE_AGENT); }
; #define XB_SPIN(cond, bar) do { unsigned _sp = 0; while (cond) { __builtin_amdgcn_s_sleep(1); \
;     if ((++_sp & 255u) == 0u) { if (xb_ld(&(bar)[XB_TMO])) break; if (_sp > XB_SPIN_CAP) { atomicAdd(&(bar)[XB_TMO], 1u); break; } } } } while (0)
; __device__ __forceinline__ void xcd_barrier(const XcdBarrier& b) {
;     ...
;         const unsigned old = xb_add(&bar[XB_XSUB(b.x)], 1u);
;         const unsigned gen = old / nloc;
;         if (old + 1u == (gen + 1u) * nloc) {
;             __builtin_amdgcn_fence(__ATOMIC_RELEASE, "agent");
;             asm volatile("s_waitcnt vmcnt(0)" ::: "memory");
;             const unsigned og = xb_add(&bar[XB_TOP], 1u);
;             const unsigned tg = og / nx;
;             if (og + 1u == (tg + 1u) * nx) xb_add(&bar[XB_TOPGEN], 1u);
;             else XB_SPIN(xb_ld(&bar[XB_TOPGEN]) == tg, bar);
;             __builtin_amdgcn_fence(__ATOMIC_ACQUIRE, "agent");
;             xb_add(&bar[XB_XGEN(b.x)], 1u);
;             asm volatile("s_waitcnt vmcnt(0)" ::: "memory");
.LBB0_240:
	s_andn2_saveexec_b64 s[4:5], s[4:5]
	s_cbranch_execz .LBB0_258
	s_mov_b64 s[4:5], exec
	buffer_wbl2 sc1
	buffer_inv sc1
	s_waitcnt lgkmcnt(0)
	s_waitcnt vmcnt(0)
	v_mov_b32_e32 v5, 0x23fc8
	ds_read_b32 v4, v5
	s_getreg_b32 s4, hwreg(HW_REG_XCC_ID, 0, 4)
	s_lshl_b32 s4, s4, 8
	s_waitcnt lgkmcnt(0)
	v_add_u32_e32 v4, 1, v4
	ds_write_b32 v5, v4
	v_mul_u32_u24_e32 v4, v4, v2
	v_mov_b32_e32 v5, s4
	v_sub_u32_e32 v5, 0x3600, v5
	v_mov_b32_e32 v6, 1
	global_atomic_add v5, v6, s[2:3]
	global_atomic_add v5, v6, s[2:3] offset:256
	global_atomic_add v5, v6, s[2:3] offset:512
	global_atomic_add v5, v6, s[2:3] offset:768
	global_atomic_add v5, v6, s[2:3] offset:1024
	global_atomic_add v5, v6, s[2:3] offset:1280
	global_atomic_add v5, v6, s[2:3] offset:1536
	global_atomic_add v5, v6, s[2:3] offset:1792
	s_nop 1
	v_add_u32_e32 v6, 1, v3
	v_mov_b32_e32 v5, 0x2000
	global_atomic_umax v5, v6, s[2:3] offset:1024
	s_nop 1
	v_mov_b32_e32 v5, 0x3200
	s_mov_b32 s5, 0
.Lxb_spin_2:
	global_load_dword v6, v5, s[2:3] offset:1024 sc1
	s_add_i32 s5, s5, 1
	s_waitcnt vmcnt(0)
	v_cmp_gt_u32_e32 vcc, v4, v6
	s_cbranch_vccz .Lxb_done_2
	s_cmp_lt_u32 s5, 0x40000
	s_cbranch_scc0 .Lxb_done_2
	s_sleep 1
	s_branch .Lxb_spin_2
.Lxb_done_2:
	s_branch .LBB0_258
	v_mbcnt_lo_u32_b32 v3, s4, 0
	v_mbcnt_hi_u32_b32 v3, s5, v3
	v_cmp_eq_u32_e32 vcc, 0, v3
	s_and_saveexec_b64 s[6:7], vcc
	s_cbranch_execz .LBB0_243
	s_bcnt1_i32_b64 s4, s[4:5]
	v_mov_b32_e32 v4, 0x7000
	v_mov_b32_e32 v5, s4
	global_atomic_add v4, v4, v5, s[94:95] offset:1024 sc0

; __device__ __forceinline__ unsigned xb_ld(unsigned* p)              { return __hip_atomic_load(p, __ATOMIC_RELAXED, __HIP_MEMORY_SCOPE_AGENT); }
; __device__ __forceinline__ unsigned xb_add(unsigned* p, unsigned v) { return __hip_atomic_fetch_add(p, v, __ATOMIC_RELAXED, __HIP_MEMORY_SCOPE_AGENT); }
; #define XB_SPIN(cond, bar) do { unsigned _sp = 0; while (cond) { __builtin_amdgcn_s_sleep(1); \
;     if ((++_sp & 255u) == 0u) { if (xb_ld(&(bar)[XB_TMO])) break; if (_sp > XB_SPIN_CAP) { atomicAdd(&(bar)[XB_TMO], 1u); break; } } } } while (0)
; __device__ __forceinline__ void xcd_barrier(const XcdBarrier& b) {
;     ...
;         unsigned nloc = b.st[0], nx = b.st[1];
;         if (nloc == 0u) { xcd_barrier_complete(bar, b.x, nloc, nx); b.st[0] = nloc; b.st[1] = nx; }
;         const unsigned old = xb_add(&bar[XB_XSUB(b.x)], 1u);
;         const unsigned gen = old / nloc;
;         if (old + 1u == (gen + 1u) * nloc) {
;             __builtin_amdgcn_fence(__ATOMIC_RELEASE, "agent");
;             asm volatile("s_waitcnt vmcnt(0)" ::: "memory");
;             const unsigned og = xb_add(&bar[XB_TOP], 1u);
;             const unsigned tg = og / nx;
;             if (og + 1u == (tg + 1u) * nx) xb_add(&bar[XB_TOPGEN], 1u);
;             else XB_SPIN(xb_ld(&bar[XB_TOPGEN]) == tg, bar);
;             __builtin_amdgcn_fence(__ATOMIC_ACQUIRE, "agent");
;             xb_add(&bar[XB_XGEN(b.x)], 1u);
;             asm volatile("s_waitcnt vmcnt(0)" ::: "memory");
;         } else {
;             XB_SPIN(xb_ld(&bar[XB_XGEN(b.x)]) == gen, bar);
;             __builtin_amdgcn_fence(__ATOMIC_ACQUIRE, "agent");
;             asm volatile("s_waitcnt vmcnt(0)" ::: "memory");
.LBB0_4431:
	v_readlane_b32 s0, v253, 6
	s_lshl_b32 s0, s0, 8
	v_readlane_b32 s4, v253, 4
	v_readlane_b32 s5, v253, 5
	s_add_u32 s0, s4, s0
	s_addc_u32 s1, s5, 0
	v_mov_b32_e32 v2, 0x1000
	v_mov_b32_e32 v4, 1
	global_atomic_add v4, v2, v4, s[0:1] offset:1024 sc0
	v_cvt_f32_u32_e32 v2, v3
	v_sub_u32_e32 v5, 0, v3
	v_rcp_iflag_f32_e32 v2, v2
	s_nop 0
	v_mul_f32_e32 v2, 0x4f7ffffe, v2
	v_cvt_u32_f32_e32 v2, v2
	v_mul_lo_u32 v5, v5, v2
	v_mul_hi_u32 v5, v2, v5
	v_add_u32_e32 v2, v2, v5
	s_waitcnt vmcnt(0)
	v_mul_hi_u32 v2, v4, v2
	v_mul_lo_u32 v5, v2, v3
	v_sub_u32_e32 v5, v4, v5
	v_add_u32_e32 v6, 1, v2
	v_cmp_ge_u32_e32 vcc, v5, v3
	v_add_u32_e32 v4, 1, v4
	s_nop 0
	v_cndmask_b32_e32 v2, v2, v6, vcc
	v_sub_u32_e32 v6, v5, v3
	v_cndmask_b32_e32 v5, v5, v6, vcc
	v_add_u32_e32 v6, 1, v2
	v_cmp_ge_u32_e32 vcc, v5, v3
	s_nop 1
	v_cndmask_b32_e32 v2, v2, v6, vcc
	v_mul_lo_u32 v5, v3, v2
	v_add_u32_e32 v3, v5, v3
	v_cmp_ne_u32_e32 vcc, v4, v3
	s_and_saveexec_b64 s[4:5], vcc
	s_xor_b64 s[4:5], exec, s[4:5]
	s_cbranch_execz .LBB0_4445
	s_waitcnt lgkmcnt(0)
	v_mov_b32_e32 v2, 0x23fc8
	ds_read_b32 v4, v2
	s_waitcnt lgkmcnt(0)
	v_add_u32_e32 v4, 1, v4
	ds_write_b32 v2, v4
	v_mul_u32_u24_e32 v2, v4, v1
	v_mov_b32_e32 v1, 0x3200
	buffer_inv sc1
	global_load_dword v1, v1, s[0:1] offset:1024 sc1
	s_add_u32 s10, s0, 0x3600
	s_addc_u32 s11, s1, 0
	s_waitcnt vmcnt(0)
	v_cmp_gt_u32_e32 vcc, v2, v1
	s_and_saveexec_b64 s[6:7], vcc
	s_cbranch_execz .LBB0_4444
	s_add_u32 s8, s94, 0x4200
	s_addc_u32 s9, s95, 0
	s_mov_b32 s22, 1
	s_mov_b64 s[12:13], 0
	v_mov_b32_e32 v1, 0
	s_branch .LBB0_4435

; __device__ __forceinline__ unsigned xb_ld(unsigned* p)              { return __hip_atomic_load(p, __ATOMIC_RELAXED, __HIP_MEMORY_SCOPE_AGENT); }
; __device__ __forceinline__ unsigned xb_add(unsigned* p, unsigned v) { return __hip_atomic_fetch_add(p, v, __ATOMIC_RELAXED, __HIP_MEMORY_SCOPE_AGENT); }
; #define XB_SPIN(cond, bar) do { unsigned _sp = 0; while (cond) { __builtin_amdgcn_s_sleep(1); \
;     if ((++_sp & 255u) == 0u) { if (xb_ld(&(bar)[XB_TMO])) break; if (_sp > XB_SPIN_CAP) { atomicAdd(&(bar)[XB_TMO], 1u); break; } } } } while (0)
; __device__ __forceinline__ void xcd_barrier(const XcdBarrier& b) {
;     ...
;         const unsigned old = xb_add(&bar[XB_XSUB(b.x)], 1u);
;         const unsigned gen = old / nloc;
;         if (old + 1u == (gen + 1u) * nloc) {
;             __builtin_amdgcn_fence(__ATOMIC_RELEASE, "agent");
;             asm volatile("s_waitcnt vmcnt(0)" ::: "memory");
;             const unsigned og = xb_add(&bar[XB_TOP], 1u);
;             const unsigned tg = og / nx;
;             if (og + 1u == (tg + 1u) * nx) xb_add(&bar[XB_TOPGEN], 1u);
;             else XB_SPIN(xb_ld(&bar[XB_TOPGEN]) == tg, bar);
;             __builtin_amdgcn_fence(__ATOMIC_ACQUIRE, "agent");
;             xb_add(&bar[XB_XGEN(b.x)], 1u);
;             asm volatile("s_waitcnt vmcnt(0)" ::: "memory");
.LBB0_4445:
	s_andn2_saveexec_b64 s[4:5], s[4:5]
	s_cbranch_execz .LBB0_4463
	s_mov_b64 s[4:5], exec
	buffer_wbl2 sc1
	buffer_inv sc1
	s_waitcnt lgkmcnt(0)
	s_waitcnt vmcnt(0)
	v_mov_b32_e32 v4, 0x23fc8
	ds_read_b32 v3, v4
	s_getreg_b32 s4, hwreg(HW_REG_XCC_ID, 0, 4)
	s_lshl_b32 s4, s4, 8
	s_waitcnt lgkmcnt(0)
	v_add_u32_e32 v3, 1, v3
	ds_write_b32 v4, v3
	v_mul_u32_u24_e32 v3, v3, v1
	v_mov_b32_e32 v4, s4
	v_sub_u32_e32 v4, 0x3600, v4
	v_mov_b32_e32 v5, 1
	global_atomic_add v4, v5, s[0:1]
	global_atomic_add v4, v5, s[0:1] offset:256
	global_atomic_add v4, v5, s[0:1] offset:512
	global_atomic_add v4, v5, s[0:1] offset:768
	global_atomic_add v4, v5, s[0:1] offset:1024
	global_atomic_add v4, v5, s[0:1] offset:1280
	global_atomic_add v4, v5, s[0:1] offset:1536
	global_atomic_add v4, v5, s[0:1] offset:1792
	s_nop 1
	v_add_u32_e32 v5, 1, v2
	v_mov_b32_e32 v4, 0x2000
	global_atomic_umax v4, v5, s[0:1] offset:1024
	s_nop 1
	v_mov_b32_e32 v4, 0x3200
	s_mov_b32 s5, 0
.Lxb_spin_30:
	global_load_dword v5, v4, s[0:1] offset:1024 sc1
	s_add_i32 s5, s5, 1
	s_waitcnt vmcnt(0)
	v_cmp_gt_u32_e32 vcc, v3, v5
	s_cbranch_vccz .Lxb_done_30
	s_cmp_lt_u32 s5, 0x40000
	s_cbranch_scc0 .Lxb_done_30
	s_sleep 1
	s_branch .Lxb_spin_30
